# E1: activations of a token fetched once per wave by LDS-DMA and read as broadcast MFMA A fragments (was 8 replicated global loads per token)
# speedup vs baseline: 1.0750x; 1.0057x over previous
.Le1w_first:
	s_mov_b64 exec, 1
	global_atomic_add v250, v211, v1, s[0:1] sc0
	s_mov_b64 exec, -1
	v_mov_b32_e32 v249, 0x80
	v_and_b32_e32 v233, 7, v0
	v_bfe_u32 v234, v0, 4, 2
	v_xor_b32_e32 v235, v233, v234
	v_lshlrev_b32_e32 v144, 4, v235
	v_xor_b32_e32 v145, 64, v144
	v_and_b32_e32 v233, 15, v0
	v_bfe_u32 v234, v0, 4, 2
	v_bfe_u32 v235, v0, 1, 3
	v_xor_b32_e32 v235, v234, v235
	v_lshlrev_b32_e32 v235, 4, v235
	v_lshl_add_u32 v235, v233, 7, v235
	v_lshrrev_b32_e32 v236, 6, v0
	s_nop 0
	v_readfirstlane_b32 s38, v236
	s_lshl_b32 s38, s38, 14
	v_add_u32_e32 v146, s38, v235
	v_xor_b32_e32 v147, 64, v146
	s_lshr_b32 s99, s38, 4
	s_add_i32 s99, s99, 0x21000
	v_bfe_u32 v234, v0, 4, 2
	v_lshl_add_u32 v148, v234, 6, s99
	s_add_u32 s2, s96, 0x4c00000
	s_addc_u32 s3, s97, 0
	s_add_u32 s4, s96, 0x27600000
	s_addc_u32 s5, s97, 0
	s_add_u32 s4, s4, s80
	s_addc_u32 s5, s5, 0
	s_lshl_b32 s33, s60, 3
	s_waitcnt vmcnt(0)
	v_readfirstlane_b32 s35, v250
	s_cmp_ge_i32 s35, s33
	s_cbranch_scc1 .LBB0_722
	s_lshr_b32 s99, s35, 3
	s_lshl_b32 s98, s99, 6
	s_and_b32 s99, s99, 0xffffff00
	s_add_i32 s99, s99, 0x100
	s_and_b64 s[24:25], s[30:31], exec
	s_cselect_b32 s99, 0, s99
	s_add_i32 s98, s98, s99
	s_and_b32 s99, s35, 7
	s_lshl_b32 s99, s99, 3
	s_add_i32 s98, s98, s99
	s_mov_b32 s39, s98
	v_bfe_u32 v234, v0, 3, 3
	s_lshl_b32 s99, s98, 8
	v_lshl_add_u32 v149, v234, 5, s99
	v_and_b32_e32 v233, 7, v0
	v_lshl_add_u32 v233, v233, 5, s99
	v_bfe_u32 v235, v0, 3, 1
	v_lshl_add_u32 v151, v235, 4, v233
	s_lshl_b32 s99, s98, 12
	s_add_i32 s99, s99, s76
	v_and_b32_e32 v234, 31, v0
	v_lshl_add_u32 v150, v234, 4, s99
	global_load_dwordx4 v[66:69], v149, s[22:23]
	global_load_dwordx4 v[70:73], v149, s[22:23] offset:16
	v_add_u32_e32 v149, 0x100, v149
	global_load_dwordx4 v[74:77], v149, s[22:23]
	global_load_dwordx4 v[78:81], v149, s[22:23] offset:16
	v_add_u32_e32 v149, 0x100, v149
	s_lshr_b32 s99, s38, 4
	s_add_i32 m0, s99, 0x21000
	s_mov_b32 exec_hi, 0
	global_load_lds_dwordx4 v150, s[2:3]
	s_mov_b32 exec_hi, -1
	v_add_u32_e32 v150, 0x1000, v150
	s_waitcnt vmcnt(3)
	s_add_i32 m0, s38, 0x0
	v_mad_u32_u16 v142, v66, v249, v144
	global_load_lds_dwordx4 v142, s[10:11]
	s_add_i32 m0, s38, 0x400
	v_mad_u32_u16 v143, v70, v249, v145
	global_load_lds_dwordx4 v143, s[10:11]
	s_add_i32 m0, s38, 0x800
	v_mad_u32_u16 v142, v66, v249, v144 op_sel:[1,0,0,0]
	global_load_lds_dwordx4 v142, s[10:11]
	s_add_i32 m0, s38, 0xc00
	v_mad_u32_u16 v143, v70, v249, v145 op_sel:[1,0,0,0]
	global_load_lds_dwordx4 v143, s[10:11]
	s_add_i32 m0, s38, 0x1000
	v_mad_u32_u16 v142, v67, v249, v144
	global_load_lds_dwordx4 v142, s[10:11]
	s_add_i32 m0, s38, 0x1400
	v_mad_u32_u16 v143, v71, v249, v145
	global_load_lds_dwordx4 v143, s[10:11]
	s_add_i32 m0, s38, 0x1800
	v_mad_u32_u16 v142, v67, v249, v144 op_sel:[1,0,0,0]
	global_load_lds_dwordx4 v142, s[10:11]
	s_add_i32 m0, s38, 0x1c00
	v_mad_u32_u16 v143, v71, v249, v145 op_sel:[1,0,0,0]
	global_load_lds_dwordx4 v143, s[10:11]
	s_add_i32 m0, s38, 0x2000
	v_mad_u32_u16 v142, v68, v249, v144
	global_load_lds_dwordx4 v142, s[10:11]
	s_add_i32 m0, s38, 0x2400
	v_mad_u32_u16 v143, v72, v249, v145
	global_load_lds_dwordx4 v143, s[10:11]
	s_add_i32 m0, s38, 0x2800
	v_mad_u32_u16 v142, v68, v249, v144 op_sel:[1,0,0,0]
	global_load_lds_dwordx4 v142, s[10:11]
	s_add_i32 m0, s38, 0x2c00
	v_mad_u32_u16 v143, v72, v249, v145 op_sel:[1,0,0,0]
	global_load_lds_dwordx4 v143, s[10:11]
	s_add_i32 m0, s38, 0x3000
	v_mad_u32_u16 v142, v69, v249, v144
	global_load_lds_dwordx4 v142, s[10:11]
	s_add_i32 m0, s38, 0x3400
	v_mad_u32_u16 v143, v73, v249, v145
	global_load_lds_dwordx4 v143, s[10:11]
	s_add_i32 m0, s38, 0x3800
	v_mad_u32_u16 v142, v69, v249, v144 op_sel:[1,0,0,0]
	global_load_lds_dwordx4 v142, s[10:11]
	s_add_i32 m0, s38, 0x3c00
	v_mad_u32_u16 v143, v73, v249, v145 op_sel:[1,0,0,0]
	global_load_lds_dwordx4 v143, s[10:11]
	s_mov_b32 s34, 0
	s_mov_b32 s43, 0
	s_waitcnt vmcnt(0)
	ds_read_b128 v[82:85], v146
	ds_read_b128 v[86:89], v147
	ds_read_b128 v[2:5], v148
	ds_read_b128 v[6:9], v148 offset:16
	ds_read_b128 v[10:13], v148 offset:32
	ds_read_b128 v[14:17], v148 offset:48
	ds_read_b128 v[18:21], v148 offset:256
	ds_read_b128 v[22:25], v148 offset:272
	ds_read_b128 v[26:29], v148 offset:288
	ds_read_b128 v[30:33], v148 offset:304

.Le1_no6:
	s_lshr_b32 s99, s38, 4
	s_add_i32 m0, s99, 0x21200
	s_mov_b32 exec_hi, 0
	global_load_lds_dwordx4 v150, s[2:3]
	s_mov_b32 exec_hi, -1
	v_add_u32_e32 v150, s40, v150
	global_load_dwordx4 v[66:69], v149, s[22:23]
	global_load_dwordx4 v[70:73], v149, s[22:23] offset:16
	v_add_u32_e32 v149, 0x100, v149
	s_waitcnt vmcnt(16)
	ds_read_b128 v[90:93], v146 offset:2048
	ds_read_b128 v[94:97], v147 offset:2048
	s_waitcnt lgkmcnt(2)
	s_add_i32 m0, s38, 0x0
	v_mad_u32_u16 v142, v74, v249, v144
	global_load_lds_dwordx4 v142, s[10:11]
	s_add_i32 m0, s38, 0x400
	v_mad_u32_u16 v143, v78, v249, v145
	global_load_lds_dwordx4 v143, s[10:11]
	v_cvt_scalef32_pk_bf16_fp4 v98, v82, 1.0
	v_cvt_scalef32_pk_bf16_fp4 v99, v82, 1.0 op_sel:[1,0,0]
	v_cvt_scalef32_pk_bf16_fp4 v100, v82, 1.0 op_sel:[0,1,0]
	v_cvt_scalef32_pk_bf16_fp4 v101, v82, 1.0 op_sel:[1,1,0]
	v_cvt_scalef32_pk_bf16_fp4 v102, v83, 1.0
	v_cvt_scalef32_pk_bf16_fp4 v103, v83, 1.0 op_sel:[1,0,0]
	v_cvt_scalef32_pk_bf16_fp4 v104, v83, 1.0 op_sel:[0,1,0]
	v_cvt_scalef32_pk_bf16_fp4 v105, v83, 1.0 op_sel:[1,1,0]
	v_mfma_f32_16x16x32_bf16 v[106:109], v[2:5], v[98:101], 0
	v_cvt_scalef32_pk_bf16_fp4 v98, v84, 1.0
	v_cvt_scalef32_pk_bf16_fp4 v99, v84, 1.0 op_sel:[1,0,0]
	v_cvt_scalef32_pk_bf16_fp4 v100, v84, 1.0 op_sel:[0,1,0]
	v_cvt_scalef32_pk_bf16_fp4 v101, v84, 1.0 op_sel:[1,1,0]
	v_mfma_f32_16x16x32_bf16 v[106:109], v[6:9], v[102:105], v[106:109]
	v_cvt_scalef32_pk_bf16_fp4 v102, v85, 1.0
	v_cvt_scalef32_pk_bf16_fp4 v103, v85, 1.0 op_sel:[1,0,0]
	v_cvt_scalef32_pk_bf16_fp4 v104, v85, 1.0 op_sel:[0,1,0]
	v_cvt_scalef32_pk_bf16_fp4 v105, v85, 1.0 op_sel:[1,1,0]
	v_mfma_f32_16x16x32_bf16 v[106:109], v[10:13], v[98:101], v[106:109]
	v_cvt_scalef32_pk_bf16_fp4 v98, v86, 1.0
	v_cvt_scalef32_pk_bf16_fp4 v99, v86, 1.0 op_sel:[1,0,0]
	v_cvt_scalef32_pk_bf16_fp4 v100, v86, 1.0 op_sel:[0,1,0]
	v_cvt_scalef32_pk_bf16_fp4 v101, v86, 1.0 op_sel:[1,1,0]
	v_mfma_f32_16x16x32_bf16 v[106:109], v[14:17], v[102:105], v[106:109]
	v_cvt_scalef32_pk_bf16_fp4 v102, v87, 1.0
	v_cvt_scalef32_pk_bf16_fp4 v103, v87, 1.0 op_sel:[1,0,0]
	v_cvt_scalef32_pk_bf16_fp4 v104, v87, 1.0 op_sel:[0,1,0]
	v_cvt_scalef32_pk_bf16_fp4 v105, v87, 1.0 op_sel:[1,1,0]
	v_mfma_f32_16x16x32_bf16 v[106:109], v[18:21], v[98:101], v[106:109]
	v_cvt_scalef32_pk_bf16_fp4 v98, v88, 1.0
	v_cvt_scalef32_pk_bf16_fp4 v99, v88, 1.0 op_sel:[1,0,0]
	v_cvt_scalef32_pk_bf16_fp4 v100, v88, 1.0 op_sel:[0,1,0]
	v_cvt_scalef32_pk_bf16_fp4 v101, v88, 1.0 op_sel:[1,1,0]
	v_mfma_f32_16x16x32_bf16 v[106:109], v[22:25], v[102:105], v[106:109]
	v_cvt_scalef32_pk_bf16_fp4 v102, v89, 1.0
	v_cvt_scalef32_pk_bf16_fp4 v103, v89, 1.0 op_sel:[1,0,0]
	v_cvt_scalef32_pk_bf16_fp4 v104, v89, 1.0 op_sel:[0,1,0]
	v_cvt_scalef32_pk_bf16_fp4 v105, v89, 1.0 op_sel:[1,1,0]
	v_mfma_f32_16x16x32_bf16 v[106:109], v[26:29], v[98:101], v[106:109]
	v_mfma_f32_16x16x32_bf16 v[106:109], v[30:33], v[102:105], v[106:109]
	s_waitcnt vmcnt(16)
	ds_read_b128 v[82:85], v146 offset:4096
	ds_read_b128 v[86:89], v147 offset:4096
	s_waitcnt lgkmcnt(2)
	s_add_i32 m0, s38, 0x800
	v_mad_u32_u16 v142, v74, v249, v144 op_sel:[1,0,0,0]
	global_load_lds_dwordx4 v142, s[10:11]
	s_add_i32 m0, s38, 0xc00
	v_mad_u32_u16 v143, v78, v249, v145 op_sel:[1,0,0,0]
	global_load_lds_dwordx4 v143, s[10:11]
	v_cvt_scalef32_pk_bf16_fp4 v98, v90, 1.0
	v_cvt_scalef32_pk_bf16_fp4 v99, v90, 1.0 op_sel:[1,0,0]
	v_cvt_scalef32_pk_bf16_fp4 v100, v90, 1.0 op_sel:[0,1,0]
	v_cvt_scalef32_pk_bf16_fp4 v101, v90, 1.0 op_sel:[1,1,0]
	v_cvt_scalef32_pk_bf16_fp4 v102, v91, 1.0
	v_cvt_scalef32_pk_bf16_fp4 v103, v91, 1.0 op_sel:[1,0,0]
	v_cvt_scalef32_pk_bf16_fp4 v104, v91, 1.0 op_sel:[0,1,0]
	v_cvt_scalef32_pk_bf16_fp4 v105, v91, 1.0 op_sel:[1,1,0]
	v_mfma_f32_16x16x32_bf16 v[110:113], v[2:5], v[98:101], 0
	v_cvt_scalef32_pk_bf16_fp4 v98, v92, 1.0
	v_cvt_scalef32_pk_bf16_fp4 v99, v92, 1.0 op_sel:[1,0,0]
	v_cvt_scalef32_pk_bf16_fp4 v100, v92, 1.0 op_sel:[0,1,0]
	v_cvt_scalef32_pk_bf16_fp4 v101, v92, 1.0 op_sel:[1,1,0]
	v_mfma_f32_16x16x32_bf16 v[110:113], v[6:9], v[102:105], v[110:113]
	v_cvt_scalef32_pk_bf16_fp4 v102, v93, 1.0
	v_cvt_scalef32_pk_bf16_fp4 v103, v93, 1.0 op_sel:[1,0,0]
	v_cvt_scalef32_pk_bf16_fp4 v104, v93, 1.0 op_sel:[0,1,0]
	v_cvt_scalef32_pk_bf16_fp4 v105, v93, 1.0 op_sel:[1,1,0]
	v_mfma_f32_16x16x32_bf16 v[110:113], v[10:13], v[98:101], v[110:113]
	v_cvt_scalef32_pk_bf16_fp4 v98, v94, 1.0
	v_cvt_scalef32_pk_bf16_fp4 v99, v94, 1.0 op_sel:[1,0,0]
	v_cvt_scalef32_pk_bf16_fp4 v100, v94, 1.0 op_sel:[0,1,0]
	v_cvt_scalef32_pk_bf16_fp4 v101, v94, 1.0 op_sel:[1,1,0]
	v_mfma_f32_16x16x32_bf16 v[110:113], v[14:17], v[102:105], v[110:113]
	v_cvt_scalef32_pk_bf16_fp4 v102, v95, 1.0
	v_cvt_scalef32_pk_bf16_fp4 v103, v95, 1.0 op_sel:[1,0,0]
	v_cvt_scalef32_pk_bf16_fp4 v104, v95, 1.0 op_sel:[0,1,0]
	v_cvt_scalef32_pk_bf16_fp4 v105, v95, 1.0 op_sel:[1,1,0]
	v_mfma_f32_16x16x32_bf16 v[110:113], v[18:21], v[98:101], v[110:113]
	v_cvt_scalef32_pk_bf16_fp4 v98, v96, 1.0
	v_cvt_scalef32_pk_bf16_fp4 v99, v96, 1.0 op_sel:[1,0,0]
	v_cvt_scalef32_pk_bf16_fp4 v100, v96, 1.0 op_sel:[0,1,0]
	v_cvt_scalef32_pk_bf16_fp4 v101, v96, 1.0 op_sel:[1,1,0]
	v_mfma_f32_16x16x32_bf16 v[110:113], v[22:25], v[102:105], v[110:113]
	v_cvt_scalef32_pk_bf16_fp4 v102, v97, 1.0
	v_cvt_scalef32_pk_bf16_fp4 v103, v97, 1.0 op_sel:[1,0,0]
	v_cvt_scalef32_pk_bf16_fp4 v104, v97, 1.0 op_sel:[0,1,0]
	v_cvt_scalef32_pk_bf16_fp4 v105, v97, 1.0 op_sel:[1,1,0]
	v_mfma_f32_16x16x32_bf16 v[110:113], v[26:29], v[98:101], v[110:113]
	v_mfma_f32_16x16x32_bf16 v[110:113], v[30:33], v[102:105], v[110:113]
	s_waitcnt vmcnt(16)
	ds_read_b128 v[90:93], v146 offset:6144
	ds_read_b128 v[94:97], v147 offset:6144
	s_waitcnt lgkmcnt(2)
	s_add_i32 m0, s38, 0x1000
	v_mad_u32_u16 v142, v75, v249, v144
	global_load_lds_dwordx4 v142, s[10:11]
	s_add_i32 m0, s38, 0x1400
	v_mad_u32_u16 v143, v79, v249, v145
	global_load_lds_dwordx4 v143, s[10:11]
	v_cvt_scalef32_pk_bf16_fp4 v98, v82, 1.0
	v_cvt_scalef32_pk_bf16_fp4 v99, v82, 1.0 op_sel:[1,0,0]
	v_cvt_scalef32_pk_bf16_fp4 v100, v82, 1.0 op_sel:[0,1,0]
	v_cvt_scalef32_pk_bf16_fp4 v101, v82, 1.0 op_sel:[1,1,0]
	v_cvt_scalef32_pk_bf16_fp4 v102, v83, 1.0
	v_cvt_scalef32_pk_bf16_fp4 v103, v83, 1.0 op_sel:[1,0,0]
	v_cvt_scalef32_pk_bf16_fp4 v104, v83, 1.0 op_sel:[0,1,0]
	v_cvt_scalef32_pk_bf16_fp4 v105, v83, 1.0 op_sel:[1,1,0]
	v_mfma_f32_16x16x32_bf16 v[114:117], v[2:5], v[98:101], 0
	v_cvt_scalef32_pk_bf16_fp4 v98, v84, 1.0
	v_cvt_scalef32_pk_bf16_fp4 v99, v84, 1.0 op_sel:[1,0,0]
	v_cvt_scalef32_pk_bf16_fp4 v100, v84, 1.0 op_sel:[0,1,0]
	v_cvt_scalef32_pk_bf16_fp4 v101, v84, 1.0 op_sel:[1,1,0]
	v_mfma_f32_16x16x32_bf16 v[114:117], v[6:9], v[102:105], v[114:117]
	v_cvt_scalef32_pk_bf16_fp4 v102, v85, 1.0
	v_cvt_scalef32_pk_bf16_fp4 v103, v85, 1.0 op_sel:[1,0,0]
	v_cvt_scalef32_pk_bf16_fp4 v104, v85, 1.0 op_sel:[0,1,0]
	v_cvt_scalef32_pk_bf16_fp4 v105, v85, 1.0 op_sel:[1,1,0]
	v_mfma_f32_16x16x32_bf16 v[114:117], v[10:13], v[98:101], v[114:117]
	v_cvt_scalef32_pk_bf16_fp4 v98, v86, 1.0
	v_cvt_scalef32_pk_bf16_fp4 v99, v86, 1.0 op_sel:[1,0,0]
	v_cvt_scalef32_pk_bf16_fp4 v100, v86, 1.0 op_sel:[0,1,0]
	v_cvt_scalef32_pk_bf16_fp4 v101, v86, 1.0 op_sel:[1,1,0]
	v_mfma_f32_16x16x32_bf16 v[114:117], v[14:17], v[102:105], v[114:117]
	v_cvt_scalef32_pk_bf16_fp4 v102, v87, 1.0
	v_cvt_scalef32_pk_bf16_fp4 v103, v87, 1.0 op_sel:[1,0,0]
	v_cvt_scalef32_pk_bf16_fp4 v104, v87, 1.0 op_sel:[0,1,0]
	v_cvt_scalef32_pk_bf16_fp4 v105, v87, 1.0 op_sel:[1,1,0]
	v_mfma_f32_16x16x32_bf16 v[114:117], v[18:21], v[98:101], v[114:117]
	v_cvt_scalef32_pk_bf16_fp4 v98, v88, 1.0
	v_cvt_scalef32_pk_bf16_fp4 v99, v88, 1.0 op_sel:[1,0,0]
	v_cvt_scalef32_pk_bf16_fp4 v100, v88, 1.0 op_sel:[0,1,0]
	v_cvt_scalef32_pk_bf16_fp4 v101, v88, 1.0 op_sel:[1,1,0]
	v_mfma_f32_16x16x32_bf16 v[114:117], v[22:25], v[102:105], v[114:117]
	v_cvt_scalef32_pk_bf16_fp4 v102, v89, 1.0
	v_cvt_scalef32_pk_bf16_fp4 v103, v89, 1.0 op_sel:[1,0,0]
	v_cvt_scalef32_pk_bf16_fp4 v104, v89, 1.0 op_sel:[0,1,0]
	v_cvt_scalef32_pk_bf16_fp4 v105, v89, 1.0 op_sel:[1,1,0]
	v_mfma_f32_16x16x32_bf16 v[114:117], v[26:29], v[98:101], v[114:117]
	v_mfma_f32_16x16x32_bf16 v[114:117], v[30:33], v[102:105], v[114:117]
	s_waitcnt vmcnt(16)
	ds_read_b128 v[82:85], v146 offset:8192
	ds_read_b128 v[86:89], v147 offset:8192
	s_waitcnt lgkmcnt(2)
	s_add_i32 m0, s38, 0x1800
	v_mad_u32_u16 v142, v75, v249, v144 op_sel:[1,0,0,0]
	global_load_lds_dwordx4 v142, s[10:11]
	s_add_i32 m0, s38, 0x1c00
	v_mad_u32_u16 v143, v79, v249, v145 op_sel:[1,0,0,0]
	global_load_lds_dwordx4 v143, s[10:11]
	v_cvt_scalef32_pk_bf16_fp4 v98, v90, 1.0
	v_cvt_scalef32_pk_bf16_fp4 v99, v90, 1.0 op_sel:[1,0,0]
	v_cvt_scalef32_pk_bf16_fp4 v100, v90, 1.0 op_sel:[0,1,0]
	v_cvt_scalef32_pk_bf16_fp4 v101, v90, 1.0 op_sel:[1,1,0]
	v_cvt_scalef32_pk_bf16_fp4 v102, v91, 1.0
	v_cvt_scalef32_pk_bf16_fp4 v103, v91, 1.0 op_sel:[1,0,0]
	v_cvt_scalef32_pk_bf16_fp4 v104, v91, 1.0 op_sel:[0,1,0]
	v_cvt_scalef32_pk_bf16_fp4 v105, v91, 1.0 op_sel:[1,1,0]
	v_mfma_f32_16x16x32_bf16 v[118:121], v[2:5], v[98:101], 0
	v_cvt_scalef32_pk_bf16_fp4 v98, v92, 1.0
	v_cvt_scalef32_pk_bf16_fp4 v99, v92, 1.0 op_sel:[1,0,0]
	v_cvt_scalef32_pk_bf16_fp4 v100, v92, 1.0 op_sel:[0,1,0]
	v_cvt_scalef32_pk_bf16_fp4 v101, v92, 1.0 op_sel:[1,1,0]
	v_mfma_f32_16x16x32_bf16 v[118:121], v[6:9], v[102:105], v[118:121]
	v_cvt_scalef32_pk_bf16_fp4 v102, v93, 1.0
	v_cvt_scalef32_pk_bf16_fp4 v103, v93, 1.0 op_sel:[1,0,0]
	v_cvt_scalef32_pk_bf16_fp4 v104, v93, 1.0 op_sel:[0,1,0]
	v_cvt_scalef32_pk_bf16_fp4 v105, v93, 1.0 op_sel:[1,1,0]
	v_mfma_f32_16x16x32_bf16 v[118:121], v[10:13], v[98:101], v[118:121]
	v_cvt_scalef32_pk_bf16_fp4 v98, v94, 1.0
	v_cvt_scalef32_pk_bf16_fp4 v99, v94, 1.0 op_sel:[1,0,0]
	v_cvt_scalef32_pk_bf16_fp4 v100, v94, 1.0 op_sel:[0,1,0]
	v_cvt_scalef32_pk_bf16_fp4 v101, v94, 1.0 op_sel:[1,1,0]
	v_mfma_f32_16x16x32_bf16 v[118:121], v[14:17], v[102:105], v[118:121]
	v_cvt_scalef32_pk_bf16_fp4 v102, v95, 1.0
	v_cvt_scalef32_pk_bf16_fp4 v103, v95, 1.0 op_sel:[1,0,0]
	v_cvt_scalef32_pk_bf16_fp4 v104, v95, 1.0 op_sel:[0,1,0]
	v_cvt_scalef32_pk_bf16_fp4 v105, v95, 1.0 op_sel:[1,1,0]
	v_mfma_f32_16x16x32_bf16 v[118:121], v[18:21], v[98:101], v[118:121]
	v_cvt_scalef32_pk_bf16_fp4 v98, v96, 1.0
	v_cvt_scalef32_pk_bf16_fp4 v99, v96, 1.0 op_sel:[1,0,0]
	v_cvt_scalef32_pk_bf16_fp4 v100, v96, 1.0 op_sel:[0,1,0]
	v_cvt_scalef32_pk_bf16_fp4 v101, v96, 1.0 op_sel:[1,1,0]
	v_mfma_f32_16x16x32_bf16 v[118:121], v[22:25], v[102:105], v[118:121]
	v_cvt_scalef32_pk_bf16_fp4 v102, v97, 1.0
	v_cvt_scalef32_pk_bf16_fp4 v103, v97, 1.0 op_sel:[1,0,0]
	v_cvt_scalef32_pk_bf16_fp4 v104, v97, 1.0 op_sel:[0,1,0]
	v_cvt_scalef32_pk_bf16_fp4 v105, v97, 1.0 op_sel:[1,1,0]
	v_mfma_f32_16x16x32_bf16 v[118:121], v[26:29], v[98:101], v[118:121]
	v_cvt_pk_bf16_f32 v138, v106, v110
	v_mfma_f32_16x16x32_bf16 v[118:121], v[30:33], v[102:105], v[118:121]
	s_waitcnt vmcnt(16)
	ds_read_b128 v[90:93], v146 offset:10240
	ds_read_b128 v[94:97], v147 offset:10240
	s_waitcnt lgkmcnt(2)
	s_add_i32 m0, s38, 0x2000
	v_mad_u32_u16 v142, v76, v249, v144
	global_load_lds_dwordx4 v142, s[10:11]
	s_add_i32 m0, s38, 0x2400
	v_mad_u32_u16 v143, v80, v249, v145
	global_load_lds_dwordx4 v143, s[10:11]
	v_cvt_scalef32_pk_bf16_fp4 v98, v82, 1.0
	v_cvt_scalef32_pk_bf16_fp4 v99, v82, 1.0 op_sel:[1,0,0]
	v_cvt_scalef32_pk_bf16_fp4 v100, v82, 1.0 op_sel:[0,1,0]
	v_cvt_scalef32_pk_bf16_fp4 v101, v82, 1.0 op_sel:[1,1,0]
	v_cvt_scalef32_pk_bf16_fp4 v102, v83, 1.0
	v_cvt_scalef32_pk_bf16_fp4 v103, v83, 1.0 op_sel:[1,0,0]
	v_cvt_scalef32_pk_bf16_fp4 v104, v83, 1.0 op_sel:[0,1,0]
	v_cvt_scalef32_pk_bf16_fp4 v105, v83, 1.0 op_sel:[1,1,0]
	v_mfma_f32_16x16x32_bf16 v[122:125], v[2:5], v[98:101], 0
	v_cvt_scalef32_pk_bf16_fp4 v98, v84, 1.0
	v_cvt_scalef32_pk_bf16_fp4 v99, v84, 1.0 op_sel:[1,0,0]
	v_cvt_scalef32_pk_bf16_fp4 v100, v84, 1.0 op_sel:[0,1,0]
	v_cvt_scalef32_pk_bf16_fp4 v101, v84, 1.0 op_sel:[1,1,0]
	v_mfma_f32_16x16x32_bf16 v[122:125], v[6:9], v[102:105], v[122:125]
	v_cvt_scalef32_pk_bf16_fp4 v102, v85, 1.0
	v_cvt_scalef32_pk_bf16_fp4 v103, v85, 1.0 op_sel:[1,0,0]
	v_cvt_scalef32_pk_bf16_fp4 v104, v85, 1.0 op_sel:[0,1,0]
	v_cvt_scalef32_pk_bf16_fp4 v105, v85, 1.0 op_sel:[1,1,0]
	v_mfma_f32_16x16x32_bf16 v[122:125], v[10:13], v[98:101], v[122:125]
	v_cvt_scalef32_pk_bf16_fp4 v98, v86, 1.0
	v_cvt_scalef32_pk_bf16_fp4 v99, v86, 1.0 op_sel:[1,0,0]
	v_cvt_scalef32_pk_bf16_fp4 v100, v86, 1.0 op_sel:[0,1,0]
	v_cvt_scalef32_pk_bf16_fp4 v101, v86, 1.0 op_sel:[1,1,0]
	v_mfma_f32_16x16x32_bf16 v[122:125], v[14:17], v[102:105], v[122:125]
	v_cvt_scalef32_pk_bf16_fp4 v102, v87, 1.0
	v_cvt_scalef32_pk_bf16_fp4 v103, v87, 1.0 op_sel:[1,0,0]
	v_cvt_scalef32_pk_bf16_fp4 v104, v87, 1.0 op_sel:[0,1,0]
	v_cvt_scalef32_pk_bf16_fp4 v105, v87, 1.0 op_sel:[1,1,0]
	v_mfma_f32_16x16x32_bf16 v[122:125], v[18:21], v[98:101], v[122:125]
	v_cvt_scalef32_pk_bf16_fp4 v98, v88, 1.0
	v_cvt_scalef32_pk_bf16_fp4 v99, v88, 1.0 op_sel:[1,0,0]
	v_cvt_scalef32_pk_bf16_fp4 v100, v88, 1.0 op_sel:[0,1,0]
	v_cvt_scalef32_pk_bf16_fp4 v101, v88, 1.0 op_sel:[1,1,0]
	v_mfma_f32_16x16x32_bf16 v[122:125], v[22:25], v[102:105], v[122:125]
	v_cvt_scalef32_pk_bf16_fp4 v102, v89, 1.0
	v_cvt_scalef32_pk_bf16_fp4 v103, v89, 1.0 op_sel:[1,0,0]
	v_cvt_scalef32_pk_bf16_fp4 v104, v89, 1.0 op_sel:[0,1,0]
	v_cvt_scalef32_pk_bf16_fp4 v105, v89, 1.0 op_sel:[1,1,0]
	v_mfma_f32_16x16x32_bf16 v[122:125], v[26:29], v[98:101], v[122:125]
	v_mfma_f32_16x16x32_bf16 v[122:125], v[30:33], v[102:105], v[122:125]
	s_waitcnt vmcnt(16)
	ds_read_b128 v[82:85], v146 offset:12288
	ds_read_b128 v[86:89], v147 offset:12288
	s_waitcnt lgkmcnt(2)
	s_add_i32 m0, s38, 0x2800
	v_mad_u32_u16 v142, v76, v249, v144 op_sel:[1,0,0,0]
	global_load_lds_dwordx4 v142, s[10:11]
	s_add_i32 m0, s38, 0x2c00
	v_mad_u32_u16 v143, v80, v249, v145 op_sel:[1,0,0,0]
	global_load_lds_dwordx4 v143, s[10:11]
	v_cvt_scalef32_pk_bf16_fp4 v98, v90, 1.0
	v_cvt_scalef32_pk_bf16_fp4 v99, v90, 1.0 op_sel:[1,0,0]
	v_cvt_scalef32_pk_bf16_fp4 v100, v90, 1.0 op_sel:[0,1,0]
	v_cvt_scalef32_pk_bf16_fp4 v101, v90, 1.0 op_sel:[1,1,0]
	v_cvt_scalef32_pk_bf16_fp4 v102, v91, 1.0
	v_cvt_scalef32_pk_bf16_fp4 v103, v91, 1.0 op_sel:[1,0,0]
	v_cvt_scalef32_pk_bf16_fp4 v104, v91, 1.0 op_sel:[0,1,0]
	v_cvt_scalef32_pk_bf16_fp4 v105, v91, 1.0 op_sel:[1,1,0]
	v_mfma_f32_16x16x32_bf16 v[126:129], v[2:5], v[98:101], 0
	v_cvt_scalef32_pk_bf16_fp4 v98, v92, 1.0
	v_cvt_scalef32_pk_bf16_fp4 v99, v92, 1.0 op_sel:[1,0,0]
	v_cvt_scalef32_pk_bf16_fp4 v100, v92, 1.0 op_sel:[0,1,0]
	v_cvt_scalef32_pk_bf16_fp4 v101, v92, 1.0 op_sel:[1,1,0]
	v_mfma_f32_16x16x32_bf16 v[126:129], v[6:9], v[102:105], v[126:129]
	v_cvt_scalef32_pk_bf16_fp4 v102, v93, 1.0
	v_cvt_scalef32_pk_bf16_fp4 v103, v93, 1.0 op_sel:[1,0,0]
	v_cvt_scalef32_pk_bf16_fp4 v104, v93, 1.0 op_sel:[0,1,0]
	v_cvt_scalef32_pk_bf16_fp4 v105, v93, 1.0 op_sel:[1,1,0]
	v_mfma_f32_16x16x32_bf16 v[126:129], v[10:13], v[98:101], v[126:129]
	v_cvt_scalef32_pk_bf16_fp4 v98, v94, 1.0
	v_cvt_scalef32_pk_bf16_fp4 v99, v94, 1.0 op_sel:[1,0,0]
	v_cvt_scalef32_pk_bf16_fp4 v100, v94, 1.0 op_sel:[0,1,0]
	v_cvt_scalef32_pk_bf16_fp4 v101, v94, 1.0 op_sel:[1,1,0]
	v_mfma_f32_16x16x32_bf16 v[126:129], v[14:17], v[102:105], v[126:129]
	v_cvt_scalef32_pk_bf16_fp4 v102, v95, 1.0
	v_cvt_scalef32_pk_bf16_fp4 v103, v95, 1.0 op_sel:[1,0,0]
	v_cvt_scalef32_pk_bf16_fp4 v104, v95, 1.0 op_sel:[0,1,0]
	v_cvt_scalef32_pk_bf16_fp4 v105, v95, 1.0 op_sel:[1,1,0]
	v_mfma_f32_16x16x32_bf16 v[126:129], v[18:21], v[98:101], v[126:129]
	v_cvt_scalef32_pk_bf16_fp4 v98, v96, 1.0
	v_cvt_scalef32_pk_bf16_fp4 v99, v96, 1.0 op_sel:[1,0,0]
	v_cvt_scalef32_pk_bf16_fp4 v100, v96, 1.0 op_sel:[0,1,0]
	v_cvt_scalef32_pk_bf16_fp4 v101, v96, 1.0 op_sel:[1,1,0]
	v_mfma_f32_16x16x32_bf16 v[126:129], v[22:25], v[102:105], v[126:129]
	v_cvt_scalef32_pk_bf16_fp4 v102, v97, 1.0
	v_cvt_scalef32_pk_bf16_fp4 v103, v97, 1.0 op_sel:[1,0,0]
	v_cvt_scalef32_pk_bf16_fp4 v104, v97, 1.0 op_sel:[0,1,0]
	v_cvt_scalef32_pk_bf16_fp4 v105, v97, 1.0 op_sel:[1,1,0]
	v_mfma_f32_16x16x32_bf16 v[126:129], v[26:29], v[98:101], v[126:129]
	v_cvt_pk_bf16_f32 v139, v114, v118
	v_mfma_f32_16x16x32_bf16 v[126:129], v[30:33], v[102:105], v[126:129]
	s_waitcnt vmcnt(16)
	ds_read_b128 v[90:93], v146 offset:14336
	ds_read_b128 v[94:97], v147 offset:14336
	s_waitcnt lgkmcnt(2)
	s_add_i32 m0, s38, 0x3000
	v_mad_u32_u16 v142, v77, v249, v144
	global_load_lds_dwordx4 v142, s[10:11]
	s_add_i32 m0, s38, 0x3400
	v_mad_u32_u16 v143, v81, v249, v145
	global_load_lds_dwordx4 v143, s[10:11]
	v_cvt_scalef32_pk_bf16_fp4 v98, v82, 1.0
	v_cvt_scalef32_pk_bf16_fp4 v99, v82, 1.0 op_sel:[1,0,0]
	v_cvt_scalef32_pk_bf16_fp4 v100, v82, 1.0 op_sel:[0,1,0]
	v_cvt_scalef32_pk_bf16_fp4 v101, v82, 1.0 op_sel:[1,1,0]
	v_cvt_scalef32_pk_bf16_fp4 v102, v83, 1.0
	v_cvt_scalef32_pk_bf16_fp4 v103, v83, 1.0 op_sel:[1,0,0]
	v_cvt_scalef32_pk_bf16_fp4 v104, v83, 1.0 op_sel:[0,1,0]
	v_cvt_scalef32_pk_bf16_fp4 v105, v83, 1.0 op_sel:[1,1,0]
	v_mfma_f32_16x16x32_bf16 v[130:133], v[2:5], v[98:101], 0
	v_cvt_scalef32_pk_bf16_fp4 v98, v84, 1.0
	v_cvt_scalef32_pk_bf16_fp4 v99, v84, 1.0 op_sel:[1,0,0]
	v_cvt_scalef32_pk_bf16_fp4 v100, v84, 1.0 op_sel:[0,1,0]
	v_cvt_scalef32_pk_bf16_fp4 v101, v84, 1.0 op_sel:[1,1,0]
	v_mfma_f32_16x16x32_bf16 v[130:133], v[6:9], v[102:105], v[130:133]
	v_cvt_scalef32_pk_bf16_fp4 v102, v85, 1.0
	v_cvt_scalef32_pk_bf16_fp4 v103, v85, 1.0 op_sel:[1,0,0]
	v_cvt_scalef32_pk_bf16_fp4 v104, v85, 1.0 op_sel:[0,1,0]
	v_cvt_scalef32_pk_bf16_fp4 v105, v85, 1.0 op_sel:[1,1,0]
	v_mfma_f32_16x16x32_bf16 v[130:133], v[10:13], v[98:101], v[130:133]
	v_cvt_scalef32_pk_bf16_fp4 v98, v86, 1.0
	v_cvt_scalef32_pk_bf16_fp4 v99, v86, 1.0 op_sel:[1,0,0]
	v_cvt_scalef32_pk_bf16_fp4 v100, v86, 1.0 op_sel:[0,1,0]
	v_cvt_scalef32_pk_bf16_fp4 v101, v86, 1.0 op_sel:[1,1,0]
	v_mfma_f32_16x16x32_bf16 v[130:133], v[14:17], v[102:105], v[130:133]
	v_cvt_scalef32_pk_bf16_fp4 v102, v87, 1.0
	v_cvt_scalef32_pk_bf16_fp4 v103, v87, 1.0 op_sel:[1,0,0]
	v_cvt_scalef32_pk_bf16_fp4 v104, v87, 1.0 op_sel:[0,1,0]
	v_cvt_scalef32_pk_bf16_fp4 v105, v87, 1.0 op_sel:[1,1,0]
	v_mfma_f32_16x16x32_bf16 v[130:133], v[18:21], v[98:101], v[130:133]
	v_cvt_scalef32_pk_bf16_fp4 v98, v88, 1.0
	v_cvt_scalef32_pk_bf16_fp4 v99, v88, 1.0 op_sel:[1,0,0]
	v_cvt_scalef32_pk_bf16_fp4 v100, v88, 1.0 op_sel:[0,1,0]
	v_cvt_scalef32_pk_bf16_fp4 v101, v88, 1.0 op_sel:[1,1,0]
	v_mfma_f32_16x16x32_bf16 v[130:133], v[22:25], v[102:105], v[130:133]
	v_cvt_scalef32_pk_bf16_fp4 v102, v89, 1.0
	v_cvt_scalef32_pk_bf16_fp4 v103, v89, 1.0 op_sel:[1,0,0]
	v_cvt_scalef32_pk_bf16_fp4 v104, v89, 1.0 op_sel:[0,1,0]
	v_cvt_scalef32_pk_bf16_fp4 v105, v89, 1.0 op_sel:[1,1,0]
	v_mfma_f32_16x16x32_bf16 v[130:133], v[26:29], v[98:101], v[130:133]
	v_mfma_f32_16x16x32_bf16 v[130:133], v[30:33], v[102:105], v[130:133]
	s_waitcnt vmcnt(12)
	ds_read_b128 v[82:85], v146
	ds_read_b128 v[86:89], v147
	s_waitcnt lgkmcnt(2)
	s_add_i32 m0, s38, 0x3800
	v_mad_u32_u16 v142, v77, v249, v144 op_sel:[1,0,0,0]
	global_load_lds_dwordx4 v142, s[10:11]
	s_add_i32 m0, s38, 0x3c00
	v_mad_u32_u16 v143, v81, v249, v145 op_sel:[1,0,0,0]
	global_load_lds_dwordx4 v143, s[10:11]
	ds_read_b128 v[34:37], v148 offset:512
	ds_read_b128 v[38:41], v148 offset:528
	ds_read_b128 v[42:45], v148 offset:544
	ds_read_b128 v[46:49], v148 offset:560
	ds_read_b128 v[50:53], v148 offset:768
	ds_read_b128 v[54:57], v148 offset:784
	ds_read_b128 v[58:61], v148 offset:800
	ds_read_b128 v[62:65], v148 offset:816
	v_cvt_scalef32_pk_bf16_fp4 v98, v90, 1.0
	v_cvt_scalef32_pk_bf16_fp4 v99, v90, 1.0 op_sel:[1,0,0]
	v_cvt_scalef32_pk_bf16_fp4 v100, v90, 1.0 op_sel:[0,1,0]
	v_cvt_scalef32_pk_bf16_fp4 v101, v90, 1.0 op_sel:[1,1,0]
	v_cvt_scalef32_pk_bf16_fp4 v102, v91, 1.0
	v_cvt_scalef32_pk_bf16_fp4 v103, v91, 1.0 op_sel:[1,0,0]
	v_cvt_scalef32_pk_bf16_fp4 v104, v91, 1.0 op_sel:[0,1,0]
	v_cvt_scalef32_pk_bf16_fp4 v105, v91, 1.0 op_sel:[1,1,0]
	v_mfma_f32_16x16x32_bf16 v[134:137], v[2:5], v[98:101], 0
	v_cvt_scalef32_pk_bf16_fp4 v98, v92, 1.0
	v_cvt_scalef32_pk_bf16_fp4 v99, v92, 1.0 op_sel:[1,0,0]
	v_cvt_scalef32_pk_bf16_fp4 v100, v92, 1.0 op_sel:[0,1,0]
	v_cvt_scalef32_pk_bf16_fp4 v101, v92, 1.0 op_sel:[1,1,0]
	v_mfma_f32_16x16x32_bf16 v[134:137], v[6:9], v[102:105], v[134:137]
	v_cvt_scalef32_pk_bf16_fp4 v102, v93, 1.0
	v_cvt_scalef32_pk_bf16_fp4 v103, v93, 1.0 op_sel:[1,0,0]
	v_cvt_scalef32_pk_bf16_fp4 v104, v93, 1.0 op_sel:[0,1,0]
	v_cvt_scalef32_pk_bf16_fp4 v105, v93, 1.0 op_sel:[1,1,0]
	v_mfma_f32_16x16x32_bf16 v[134:137], v[10:13], v[98:101], v[134:137]
	v_cvt_scalef32_pk_bf16_fp4 v98, v94, 1.0
	v_cvt_scalef32_pk_bf16_fp4 v99, v94, 1.0 op_sel:[1,0,0]
	v_cvt_scalef32_pk_bf16_fp4 v100, v94, 1.0 op_sel:[0,1,0]
	v_cvt_scalef32_pk_bf16_fp4 v101, v94, 1.0 op_sel:[1,1,0]
	v_mfma_f32_16x16x32_bf16 v[134:137], v[14:17], v[102:105], v[134:137]
	v_cvt_scalef32_pk_bf16_fp4 v102, v95, 1.0
	v_cvt_scalef32_pk_bf16_fp4 v103, v95, 1.0 op_sel:[1,0,0]
	v_cvt_scalef32_pk_bf16_fp4 v104, v95, 1.0 op_sel:[0,1,0]
	v_cvt_scalef32_pk_bf16_fp4 v105, v95, 1.0 op_sel:[1,1,0]
	v_mfma_f32_16x16x32_bf16 v[134:137], v[18:21], v[98:101], v[134:137]
	v_cvt_scalef32_pk_bf16_fp4 v98, v96, 1.0
	v_cvt_scalef32_pk_bf16_fp4 v99, v96, 1.0 op_sel:[1,0,0]
	v_cvt_scalef32_pk_bf16_fp4 v100, v96, 1.0 op_sel:[0,1,0]
	v_cvt_scalef32_pk_bf16_fp4 v101, v96, 1.0 op_sel:[1,1,0]
	v_mfma_f32_16x16x32_bf16 v[134:137], v[22:25], v[102:105], v[134:137]
	v_cvt_scalef32_pk_bf16_fp4 v102, v97, 1.0
	v_cvt_scalef32_pk_bf16_fp4 v103, v97, 1.0 op_sel:[1,0,0]
	v_cvt_scalef32_pk_bf16_fp4 v104, v97, 1.0 op_sel:[0,1,0]
	v_cvt_scalef32_pk_bf16_fp4 v105, v97, 1.0 op_sel:[1,1,0]
	v_mfma_f32_16x16x32_bf16 v[134:137], v[26:29], v[98:101], v[134:137]
	v_cvt_pk_bf16_f32 v140, v122, v126
	v_mfma_f32_16x16x32_bf16 v[134:137], v[30:33], v[102:105], v[134:137]
	s_nop 7
	s_nop 7
	v_cvt_pk_bf16_f32 v141, v130, v134
	s_mov_b64 exec, 0xffff
	global_store_dwordx4 v151, v[138:141], s[4:5]
	s_mov_b64 exec, -1
	v_add_u32_e32 v151, 0x100, v151
	s_lshr_b32 s99, s38, 4
	s_add_i32 m0, s99, 0x21000
	s_mov_b32 exec_hi, 0
	global_load_lds_dwordx4 v150, s[2:3]
	s_mov_b32 exec_hi, -1
	v_add_u32_e32 v150, 0x1000, v150
	global_load_dwordx4 v[74:77], v149, s[22:23]
	global_load_dwordx4 v[78:81], v149, s[22:23] offset:16
	v_add_u32_e32 v149, s41, v149
	s_waitcnt vmcnt(16)
	ds_read_b128 v[90:93], v146 offset:2048
	ds_read_b128 v[94:97], v147 offset:2048
	s_waitcnt lgkmcnt(2)
	s_add_i32 m0, s38, 0x0
	v_mad_u32_u16 v142, v66, v249, v144
	global_load_lds_dwordx4 v142, s[10:11]
	s_add_i32 m0, s38, 0x400
	v_mad_u32_u16 v143, v70, v249, v145
	global_load_lds_dwordx4 v143, s[10:11]
	v_cvt_scalef32_pk_bf16_fp4 v98, v82, 1.0
	v_cvt_scalef32_pk_bf16_fp4 v99, v82, 1.0 op_sel:[1,0,0]
	v_cvt_scalef32_pk_bf16_fp4 v100, v82, 1.0 op_sel:[0,1,0]
	v_cvt_scalef32_pk_bf16_fp4 v101, v82, 1.0 op_sel:[1,1,0]
	v_cvt_scalef32_pk_bf16_fp4 v102, v83, 1.0
	v_cvt_scalef32_pk_bf16_fp4 v103, v83, 1.0 op_sel:[1,0,0]
	v_cvt_scalef32_pk_bf16_fp4 v104, v83, 1.0 op_sel:[0,1,0]
	v_cvt_scalef32_pk_bf16_fp4 v105, v83, 1.0 op_sel:[1,1,0]
	v_mfma_f32_16x16x32_bf16 v[106:109], v[34:37], v[98:101], 0
	v_cvt_scalef32_pk_bf16_fp4 v98, v84, 1.0
	v_cvt_scalef32_pk_bf16_fp4 v99, v84, 1.0 op_sel:[1,0,0]
	v_cvt_scalef32_pk_bf16_fp4 v100, v84, 1.0 op_sel:[0,1,0]
	v_cvt_scalef32_pk_bf16_fp4 v101, v84, 1.0 op_sel:[1,1,0]
	v_mfma_f32_16x16x32_bf16 v[106:109], v[38:41], v[102:105], v[106:109]
	v_cvt_scalef32_pk_bf16_fp4 v102, v85, 1.0
	v_cvt_scalef32_pk_bf16_fp4 v103, v85, 1.0 op_sel:[1,0,0]
	v_cvt_scalef32_pk_bf16_fp4 v104, v85, 1.0 op_sel:[0,1,0]
	v_cvt_scalef32_pk_bf16_fp4 v105, v85, 1.0 op_sel:[1,1,0]
	v_mfma_f32_16x16x32_bf16 v[106:109], v[42:45], v[98:101], v[106:109]
	v_cvt_scalef32_pk_bf16_fp4 v98, v86, 1.0
	v_cvt_scalef32_pk_bf16_fp4 v99, v86, 1.0 op_sel:[1,0,0]
	v_cvt_scalef32_pk_bf16_fp4 v100, v86, 1.0 op_sel:[0,1,0]
	v_cvt_scalef32_pk_bf16_fp4 v101, v86, 1.0 op_sel:[1,1,0]
	v_mfma_f32_16x16x32_bf16 v[106:109], v[46:49], v[102:105], v[106:109]
	v_cvt_scalef32_pk_bf16_fp4 v102, v87, 1.0
	v_cvt_scalef32_pk_bf16_fp4 v103, v87, 1.0 op_sel:[1,0,0]
	v_cvt_scalef32_pk_bf16_fp4 v104, v87, 1.0 op_sel:[0,1,0]
	v_cvt_scalef32_pk_bf16_fp4 v105, v87, 1.0 op_sel:[1,1,0]
	v_mfma_f32_16x16x32_bf16 v[106:109], v[50:53], v[98:101], v[106:109]
	v_cvt_scalef32_pk_bf16_fp4 v98, v88, 1.0
	v_cvt_scalef32_pk_bf16_fp4 v99, v88, 1.0 op_sel:[1,0,0]
	v_cvt_scalef32_pk_bf16_fp4 v100, v88, 1.0 op_sel:[0,1,0]
	v_cvt_scalef32_pk_bf16_fp4 v101, v88, 1.0 op_sel:[1,1,0]
	v_mfma_f32_16x16x32_bf16 v[106:109], v[54:57], v[102:105], v[106:109]
	v_cvt_scalef32_pk_bf16_fp4 v102, v89, 1.0
	v_cvt_scalef32_pk_bf16_fp4 v103, v89, 1.0 op_sel:[1,0,0]
	v_cvt_scalef32_pk_bf16_fp4 v104, v89, 1.0 op_sel:[0,1,0]
	v_cvt_scalef32_pk_bf16_fp4 v105, v89, 1.0 op_sel:[1,1,0]
	v_mfma_f32_16x16x32_bf16 v[106:109], v[58:61], v[98:101], v[106:109]
	v_mfma_f32_16x16x32_bf16 v[106:109], v[62:65], v[102:105], v[106:109]
	s_waitcnt vmcnt(16)
	ds_read_b128 v[82:85], v146 offset:4096
	ds_read_b128 v[86:89], v147 offset:4096
	s_waitcnt lgkmcnt(2)
	s_add_i32 m0, s38, 0x800
	v_mad_u32_u16 v142, v66, v249, v144 op_sel:[1,0,0,0]
	global_load_lds_dwordx4 v142, s[10:11]
	s_add_i32 m0, s38, 0xc00
	v_mad_u32_u16 v143, v70, v249, v145 op_sel:[1,0,0,0]
	global_load_lds_dwordx4 v143, s[10:11]
	v_cvt_scalef32_pk_bf16_fp4 v98, v90, 1.0
	v_cvt_scalef32_pk_bf16_fp4 v99, v90, 1.0 op_sel:[1,0,0]
	v_cvt_scalef32_pk_bf16_fp4 v100, v90, 1.0 op_sel:[0,1,0]
	v_cvt_scalef32_pk_bf16_fp4 v101, v90, 1.0 op_sel:[1,1,0]
	v_cvt_scalef32_pk_bf16_fp4 v102, v91, 1.0
	v_cvt_scalef32_pk_bf16_fp4 v103, v91, 1.0 op_sel:[1,0,0]
	v_cvt_scalef32_pk_bf16_fp4 v104, v91, 1.0 op_sel:[0,1,0]
	v_cvt_scalef32_pk_bf16_fp4 v105, v91, 1.0 op_sel:[1,1,0]
	v_mfma_f32_16x16x32_bf16 v[110:113], v[34:37], v[98:101], 0
	v_cvt_scalef32_pk_bf16_fp4 v98, v92, 1.0
	v_cvt_scalef32_pk_bf16_fp4 v99, v92, 1.0 op_sel:[1,0,0]
	v_cvt_scalef32_pk_bf16_fp4 v100, v92, 1.0 op_sel:[0,1,0]
	v_cvt_scalef32_pk_bf16_fp4 v101, v92, 1.0 op_sel:[1,1,0]
	v_mfma_f32_16x16x32_bf16 v[110:113], v[38:41], v[102:105], v[110:113]
	v_cvt_scalef32_pk_bf16_fp4 v102, v93, 1.0
	v_cvt_scalef32_pk_bf16_fp4 v103, v93, 1.0 op_sel:[1,0,0]
	v_cvt_scalef32_pk_bf16_fp4 v104, v93, 1.0 op_sel:[0,1,0]
	v_cvt_scalef32_pk_bf16_fp4 v105, v93, 1.0 op_sel:[1,1,0]
	v_mfma_f32_16x16x32_bf16 v[110:113], v[42:45], v[98:101], v[110:113]
	v_cvt_scalef32_pk_bf16_fp4 v98, v94, 1.0
	v_cvt_scalef32_pk_bf16_fp4 v99, v94, 1.0 op_sel:[1,0,0]
	v_cvt_scalef32_pk_bf16_fp4 v100, v94, 1.0 op_sel:[0,1,0]
	v_cvt_scalef32_pk_bf16_fp4 v101, v94, 1.0 op_sel:[1,1,0]
	v_mfma_f32_16x16x32_bf16 v[110:113], v[46:49], v[102:105], v[110:113]
	v_cvt_scalef32_pk_bf16_fp4 v102, v95, 1.0
	v_cvt_scalef32_pk_bf16_fp4 v103, v95, 1.0 op_sel:[1,0,0]
	v_cvt_scalef32_pk_bf16_fp4 v104, v95, 1.0 op_sel:[0,1,0]
	v_cvt_scalef32_pk_bf16_fp4 v105, v95, 1.0 op_sel:[1,1,0]
	v_mfma_f32_16x16x32_bf16 v[110:113], v[50:53], v[98:101], v[110:113]
	v_cvt_scalef32_pk_bf16_fp4 v98, v96, 1.0
	v_cvt_scalef32_pk_bf16_fp4 v99, v96, 1.0 op_sel:[1,0,0]
	v_cvt_scalef32_pk_bf16_fp4 v100, v96, 1.0 op_sel:[0,1,0]
	v_cvt_scalef32_pk_bf16_fp4 v101, v96, 1.0 op_sel:[1,1,0]
	v_mfma_f32_16x16x32_bf16 v[110:113], v[54:57], v[102:105], v[110:113]
	v_cvt_scalef32_pk_bf16_fp4 v102, v97, 1.0
	v_cvt_scalef32_pk_bf16_fp4 v103, v97, 1.0 op_sel:[1,0,0]
	v_cvt_scalef32_pk_bf16_fp4 v104, v97, 1.0 op_sel:[0,1,0]
	v_cvt_scalef32_pk_bf16_fp4 v105, v97, 1.0 op_sel:[1,1,0]
	v_mfma_f32_16x16x32_bf16 v[110:113], v[58:61], v[98:101], v[110:113]
	v_mfma_f32_16x16x32_bf16 v[110:113], v[62:65], v[102:105], v[110:113]
	s_waitcnt vmcnt(16)
	ds_read_b128 v[90:93], v146 offset:6144
	ds_read_b128 v[94:97], v147 offset:6144
	s_waitcnt lgkmcnt(2)
	s_add_i32 m0, s38, 0x1000
	v_mad_u32_u16 v142, v67, v249, v144
	global_load_lds_dwordx4 v142, s[10:11]
	s_add_i32 m0, s38, 0x1400
	v_mad_u32_u16 v143, v71, v249, v145
	global_load_lds_dwordx4 v143, s[10:11]
	v_cvt_scalef32_pk_bf16_fp4 v98, v82, 1.0
	v_cvt_scalef32_pk_bf16_fp4 v99, v82, 1.0 op_sel:[1,0,0]
	v_cvt_scalef32_pk_bf16_fp4 v100, v82, 1.0 op_sel:[0,1,0]
	v_cvt_scalef32_pk_bf16_fp4 v101, v82, 1.0 op_sel:[1,1,0]
	v_cvt_scalef32_pk_bf16_fp4 v102, v83, 1.0
	v_cvt_scalef32_pk_bf16_fp4 v103, v83, 1.0 op_sel:[1,0,0]
	v_cvt_scalef32_pk_bf16_fp4 v104, v83, 1.0 op_sel:[0,1,0]
	v_cvt_scalef32_pk_bf16_fp4 v105, v83, 1.0 op_sel:[1,1,0]
	v_mfma_f32_16x16x32_bf16 v[114:117], v[34:37], v[98:101], 0
	v_cvt_scalef32_pk_bf16_fp4 v98, v84, 1.0
	v_cvt_scalef32_pk_bf16_fp4 v99, v84, 1.0 op_sel:[1,0,0]
	v_cvt_scalef32_pk_bf16_fp4 v100, v84, 1.0 op_sel:[0,1,0]
	v_cvt_scalef32_pk_bf16_fp4 v101, v84, 1.0 op_sel:[1,1,0]
	v_mfma_f32_16x16x32_bf16 v[114:117], v[38:41], v[102:105], v[114:117]
	v_cvt_scalef32_pk_bf16_fp4 v102, v85, 1.0
	v_cvt_scalef32_pk_bf16_fp4 v103, v85, 1.0 op_sel:[1,0,0]
	v_cvt_scalef32_pk_bf16_fp4 v104, v85, 1.0 op_sel:[0,1,0]
	v_cvt_scalef32_pk_bf16_fp4 v105, v85, 1.0 op_sel:[1,1,0]
	v_mfma_f32_16x16x32_bf16 v[114:117], v[42:45], v[98:101], v[114:117]
	v_cvt_scalef32_pk_bf16_fp4 v98, v86, 1.0
	v_cvt_scalef32_pk_bf16_fp4 v99, v86, 1.0 op_sel:[1,0,0]
	v_cvt_scalef32_pk_bf16_fp4 v100, v86, 1.0 op_sel:[0,1,0]
	v_cvt_scalef32_pk_bf16_fp4 v101, v86, 1.0 op_sel:[1,1,0]
	v_mfma_f32_16x16x32_bf16 v[114:117], v[46:49], v[102:105], v[114:117]
	v_cvt_scalef32_pk_bf16_fp4 v102, v87, 1.0
	v_cvt_scalef32_pk_bf16_fp4 v103, v87, 1.0 op_sel:[1,0,0]
	v_cvt_scalef32_pk_bf16_fp4 v104, v87, 1.0 op_sel:[0,1,0]
	v_cvt_scalef32_pk_bf16_fp4 v105, v87, 1.0 op_sel:[1,1,0]
	v_mfma_f32_16x16x32_bf16 v[114:117], v[50:53], v[98:101], v[114:117]
	v_cvt_scalef32_pk_bf16_fp4 v98, v88, 1.0
	v_cvt_scalef32_pk_bf16_fp4 v99, v88, 1.0 op_sel:[1,0,0]
	v_cvt_scalef32_pk_bf16_fp4 v100, v88, 1.0 op_sel:[0,1,0]
	v_cvt_scalef32_pk_bf16_fp4 v101, v88, 1.0 op_sel:[1,1,0]
	v_mfma_f32_16x16x32_bf16 v[114:117], v[54:57], v[102:105], v[114:117]
	v_cvt_scalef32_pk_bf16_fp4 v102, v89, 1.0
	v_cvt_scalef32_pk_bf16_fp4 v103, v89, 1.0 op_sel:[1,0,0]
	v_cvt_scalef32_pk_bf16_fp4 v104, v89, 1.0 op_sel:[0,1,0]
	v_cvt_scalef32_pk_bf16_fp4 v105, v89, 1.0 op_sel:[1,1,0]
	v_mfma_f32_16x16x32_bf16 v[114:117], v[58:61], v[98:101], v[114:117]
	v_mfma_f32_16x16x32_bf16 v[114:117], v[62:65], v[102:105], v[114:117]
	s_waitcnt vmcnt(16)
	ds_read_b128 v[82:85], v146 offset:8192
	ds_read_b128 v[86:89], v147 offset:8192
	s_waitcnt lgkmcnt(2)
	s_add_i32 m0, s38, 0x1800
	v_mad_u32_u16 v142, v67, v249, v144 op_sel:[1,0,0,0]
	global_load_lds_dwordx4 v142, s[10:11]
	s_add_i32 m0, s38, 0x1c00
	v_mad_u32_u16 v143, v71, v249, v145 op_sel:[1,0,0,0]
	global_load_lds_dwordx4 v143, s[10:11]
	v_cvt_scalef32_pk_bf16_fp4 v98, v90, 1.0
	v_cvt_scalef32_pk_bf16_fp4 v99, v90, 1.0 op_sel:[1,0,0]
	v_cvt_scalef32_pk_bf16_fp4 v100, v90, 1.0 op_sel:[0,1,0]
	v_cvt_scalef32_pk_bf16_fp4 v101, v90, 1.0 op_sel:[1,1,0]
	v_cvt_scalef32_pk_bf16_fp4 v102, v91, 1.0
	v_cvt_scalef32_pk_bf16_fp4 v103, v91, 1.0 op_sel:[1,0,0]
	v_cvt_scalef32_pk_bf16_fp4 v104, v91, 1.0 op_sel:[0,1,0]
	v_cvt_scalef32_pk_bf16_fp4 v105, v91, 1.0 op_sel:[1,1,0]
	v_mfma_f32_16x16x32_bf16 v[118:121], v[34:37], v[98:101], 0
	v_cvt_scalef32_pk_bf16_fp4 v98, v92, 1.0
	v_cvt_scalef32_pk_bf16_fp4 v99, v92, 1.0 op_sel:[1,0,0]
	v_cvt_scalef32_pk_bf16_fp4 v100, v92, 1.0 op_sel:[0,1,0]
	v_cvt_scalef32_pk_bf16_fp4 v101, v92, 1.0 op_sel:[1,1,0]
	v_mfma_f32_16x16x32_bf16 v[118:121], v[38:41], v[102:105], v[118:121]
	v_cvt_scalef32_pk_bf16_fp4 v102, v93, 1.0
	v_cvt_scalef32_pk_bf16_fp4 v103, v93, 1.0 op_sel:[1,0,0]
	v_cvt_scalef32_pk_bf16_fp4 v104, v93, 1.0 op_sel:[0,1,0]
	v_cvt_scalef32_pk_bf16_fp4 v105, v93, 1.0 op_sel:[1,1,0]
	v_mfma_f32_16x16x32_bf16 v[118:121], v[42:45], v[98:101], v[118:121]
	v_cvt_scalef32_pk_bf16_fp4 v98, v94, 1.0
	v_cvt_scalef32_pk_bf16_fp4 v99, v94, 1.0 op_sel:[1,0,0]
	v_cvt_scalef32_pk_bf16_fp4 v100, v94, 1.0 op_sel:[0,1,0]
	v_cvt_scalef32_pk_bf16_fp4 v101, v94, 1.0 op_sel:[1,1,0]
	v_mfma_f32_16x16x32_bf16 v[118:121], v[46:49], v[102:105], v[118:121]
	v_cvt_scalef32_pk_bf16_fp4 v102, v95, 1.0
	v_cvt_scalef32_pk_bf16_fp4 v103, v95, 1.0 op_sel:[1,0,0]
	v_cvt_scalef32_pk_bf16_fp4 v104, v95, 1.0 op_sel:[0,1,0]
	v_cvt_scalef32_pk_bf16_fp4 v105, v95, 1.0 op_sel:[1,1,0]
	v_mfma_f32_16x16x32_bf16 v[118:121], v[50:53], v[98:101], v[118:121]
	v_cvt_scalef32_pk_bf16_fp4 v98, v96, 1.0
	v_cvt_scalef32_pk_bf16_fp4 v99, v96, 1.0 op_sel:[1,0,0]
	v_cvt_scalef32_pk_bf16_fp4 v100, v96, 1.0 op_sel:[0,1,0]
	v_cvt_scalef32_pk_bf16_fp4 v101, v96, 1.0 op_sel:[1,1,0]
	v_mfma_f32_16x16x32_bf16 v[118:121], v[54:57], v[102:105], v[118:121]
	v_cvt_scalef32_pk_bf16_fp4 v102, v97, 1.0
	v_cvt_scalef32_pk_bf16_fp4 v103, v97, 1.0 op_sel:[1,0,0]
	v_cvt_scalef32_pk_bf16_fp4 v104, v97, 1.0 op_sel:[0,1,0]
	v_cvt_scalef32_pk_bf16_fp4 v105, v97, 1.0 op_sel:[1,1,0]
	v_mfma_f32_16x16x32_bf16 v[118:121], v[58:61], v[98:101], v[118:121]
	v_cvt_pk_bf16_f32 v138, v106, v110
	v_mfma_f32_16x16x32_bf16 v[118:121], v[62:65], v[102:105], v[118:121]
	s_waitcnt vmcnt(16)
	ds_read_b128 v[90:93], v146 offset:10240
	ds_read_b128 v[94:97], v147 offset:10240
	s_waitcnt lgkmcnt(2)
	s_add_i32 m0, s38, 0x2000
	v_mad_u32_u16 v142, v68, v249, v144
	global_load_lds_dwordx4 v142, s[10:11]
	s_add_i32 m0, s38, 0x2400
	v_mad_u32_u16 v143, v72, v249, v145
	global_load_lds_dwordx4 v143, s[10:11]
	v_cvt_scalef32_pk_bf16_fp4 v98, v82, 1.0
	v_cvt_scalef32_pk_bf16_fp4 v99, v82, 1.0 op_sel:[1,0,0]
	v_cvt_scalef32_pk_bf16_fp4 v100, v82, 1.0 op_sel:[0,1,0]
	v_cvt_scalef32_pk_bf16_fp4 v101, v82, 1.0 op_sel:[1,1,0]
	v_cvt_scalef32_pk_bf16_fp4 v102, v83, 1.0
	v_cvt_scalef32_pk_bf16_fp4 v103, v83, 1.0 op_sel:[1,0,0]
	v_cvt_scalef32_pk_bf16_fp4 v104, v83, 1.0 op_sel:[0,1,0]
	v_cvt_scalef32_pk_bf16_fp4 v105, v83, 1.0 op_sel:[1,1,0]
	v_mfma_f32_16x16x32_bf16 v[122:125], v[34:37], v[98:101], 0
	v_cvt_scalef32_pk_bf16_fp4 v98, v84, 1.0
	v_cvt_scalef32_pk_bf16_fp4 v99, v84, 1.0 op_sel:[1,0,0]
	v_cvt_scalef32_pk_bf16_fp4 v100, v84, 1.0 op_sel:[0,1,0]
	v_cvt_scalef32_pk_bf16_fp4 v101, v84, 1.0 op_sel:[1,1,0]
	v_mfma_f32_16x16x32_bf16 v[122:125], v[38:41], v[102:105], v[122:125]
	v_cvt_scalef32_pk_bf16_fp4 v102, v85, 1.0
	v_cvt_scalef32_pk_bf16_fp4 v103, v85, 1.0 op_sel:[1,0,0]
	v_cvt_scalef32_pk_bf16_fp4 v104, v85, 1.0 op_sel:[0,1,0]
	v_cvt_scalef32_pk_bf16_fp4 v105, v85, 1.0 op_sel:[1,1,0]
	v_mfma_f32_16x16x32_bf16 v[122:125], v[42:45], v[98:101], v[122:125]
	v_cvt_scalef32_pk_bf16_fp4 v98, v86, 1.0
	v_cvt_scalef32_pk_bf16_fp4 v99, v86, 1.0 op_sel:[1,0,0]
	v_cvt_scalef32_pk_bf16_fp4 v100, v86, 1.0 op_sel:[0,1,0]
	v_cvt_scalef32_pk_bf16_fp4 v101, v86, 1.0 op_sel:[1,1,0]
	v_mfma_f32_16x16x32_bf16 v[122:125], v[46:49], v[102:105], v[122:125]
	v_cvt_scalef32_pk_bf16_fp4 v102, v87, 1.0
	v_cvt_scalef32_pk_bf16_fp4 v103, v87, 1.0 op_sel:[1,0,0]
	v_cvt_scalef32_pk_bf16_fp4 v104, v87, 1.0 op_sel:[0,1,0]
	v_cvt_scalef32_pk_bf16_fp4 v105, v87, 1.0 op_sel:[1,1,0]
	v_mfma_f32_16x16x32_bf16 v[122:125], v[50:53], v[98:101], v[122:125]
	v_cvt_scalef32_pk_bf16_fp4 v98, v88, 1.0
	v_cvt_scalef32_pk_bf16_fp4 v99, v88, 1.0 op_sel:[1,0,0]
	v_cvt_scalef32_pk_bf16_fp4 v100, v88, 1.0 op_sel:[0,1,0]
	v_cvt_scalef32_pk_bf16_fp4 v101, v88, 1.0 op_sel:[1,1,0]
	v_mfma_f32_16x16x32_bf16 v[122:125], v[54:57], v[102:105], v[122:125]
	v_cvt_scalef32_pk_bf16_fp4 v102, v89, 1.0
	v_cvt_scalef32_pk_bf16_fp4 v103, v89, 1.0 op_sel:[1,0,0]
	v_cvt_scalef32_pk_bf16_fp4 v104, v89, 1.0 op_sel:[0,1,0]
	v_cvt_scalef32_pk_bf16_fp4 v105, v89, 1.0 op_sel:[1,1,0]
	v_mfma_f32_16x16x32_bf16 v[122:125], v[58:61], v[98:101], v[122:125]
	v_mfma_f32_16x16x32_bf16 v[122:125], v[62:65], v[102:105], v[122:125]
	s_waitcnt vmcnt(16)
	ds_read_b128 v[82:85], v146 offset:12288
	ds_read_b128 v[86:89], v147 offset:12288
	s_waitcnt lgkmcnt(2)
	s_add_i32 m0, s38, 0x2800
	v_mad_u32_u16 v142, v68, v249, v144 op_sel:[1,0,0,0]
	global_load_lds_dwordx4 v142, s[10:11]
	s_add_i32 m0, s38, 0x2c00
	v_mad_u32_u16 v143, v72, v249, v145 op_sel:[1,0,0,0]
	global_load_lds_dwordx4 v143, s[10:11]
	v_cvt_scalef32_pk_bf16_fp4 v98, v90, 1.0
	v_cvt_scalef32_pk_bf16_fp4 v99, v90, 1.0 op_sel:[1,0,0]
	v_cvt_scalef32_pk_bf16_fp4 v100, v90, 1.0 op_sel:[0,1,0]
	v_cvt_scalef32_pk_bf16_fp4 v101, v90, 1.0 op_sel:[1,1,0]
	v_cvt_scalef32_pk_bf16_fp4 v102, v91, 1.0
	v_cvt_scalef32_pk_bf16_fp4 v103, v91, 1.0 op_sel:[1,0,0]
	v_cvt_scalef32_pk_bf16_fp4 v104, v91, 1.0 op_sel:[0,1,0]
	v_cvt_scalef32_pk_bf16_fp4 v105, v91, 1.0 op_sel:[1,1,0]
	v_mfma_f32_16x16x32_bf16 v[126:129], v[34:37], v[98:101], 0
	v_cvt_scalef32_pk_bf16_fp4 v98, v92, 1.0
	v_cvt_scalef32_pk_bf16_fp4 v99, v92, 1.0 op_sel:[1,0,0]
	v_cvt_scalef32_pk_bf16_fp4 v100, v92, 1.0 op_sel:[0,1,0]
	v_cvt_scalef32_pk_bf16_fp4 v101, v92, 1.0 op_sel:[1,1,0]
	v_mfma_f32_16x16x32_bf16 v[126:129], v[38:41], v[102:105], v[126:129]
	v_cvt_scalef32_pk_bf16_fp4 v102, v93, 1.0
	v_cvt_scalef32_pk_bf16_fp4 v103, v93, 1.0 op_sel:[1,0,0]
	v_cvt_scalef32_pk_bf16_fp4 v104, v93, 1.0 op_sel:[0,1,0]
	v_cvt_scalef32_pk_bf16_fp4 v105, v93, 1.0 op_sel:[1,1,0]
	v_mfma_f32_16x16x32_bf16 v[126:129], v[42:45], v[98:101], v[126:129]
	v_cvt_scalef32_pk_bf16_fp4 v98, v94, 1.0
	v_cvt_scalef32_pk_bf16_fp4 v99, v94, 1.0 op_sel:[1,0,0]
	v_cvt_scalef32_pk_bf16_fp4 v100, v94, 1.0 op_sel:[0,1,0]
	v_cvt_scalef32_pk_bf16_fp4 v101, v94, 1.0 op_sel:[1,1,0]
	v_mfma_f32_16x16x32_bf16 v[126:129], v[46:49], v[102:105], v[126:129]
	v_cvt_scalef32_pk_bf16_fp4 v102, v95, 1.0
	v_cvt_scalef32_pk_bf16_fp4 v103, v95, 1.0 op_sel:[1,0,0]
	v_cvt_scalef32_pk_bf16_fp4 v104, v95, 1.0 op_sel:[0,1,0]
	v_cvt_scalef32_pk_bf16_fp4 v105, v95, 1.0 op_sel:[1,1,0]
	v_mfma_f32_16x16x32_bf16 v[126:129], v[50:53], v[98:101], v[126:129]
	v_cvt_scalef32_pk_bf16_fp4 v98, v96, 1.0
	v_cvt_scalef32_pk_bf16_fp4 v99, v96, 1.0 op_sel:[1,0,0]
	v_cvt_scalef32_pk_bf16_fp4 v100, v96, 1.0 op_sel:[0,1,0]
	v_cvt_scalef32_pk_bf16_fp4 v101, v96, 1.0 op_sel:[1,1,0]
	v_mfma_f32_16x16x32_bf16 v[126:129], v[54:57], v[102:105], v[126:129]
	v_cvt_scalef32_pk_bf16_fp4 v102, v97, 1.0
	v_cvt_scalef32_pk_bf16_fp4 v103, v97, 1.0 op_sel:[1,0,0]
	v_cvt_scalef32_pk_bf16_fp4 v104, v97, 1.0 op_sel:[0,1,0]
	v_cvt_scalef32_pk_bf16_fp4 v105, v97, 1.0 op_sel:[1,1,0]
	v_mfma_f32_16x16x32_bf16 v[126:129], v[58:61], v[98:101], v[126:129]
	v_cvt_pk_bf16_f32 v139, v114, v118
	v_mfma_f32_16x16x32_bf16 v[126:129], v[62:65], v[102:105], v[126:129]
	s_waitcnt vmcnt(16)
	ds_read_b128 v[90:93], v146 offset:14336
	ds_read_b128 v[94:97], v147 offset:14336
	s_waitcnt lgkmcnt(2)
	s_add_i32 m0, s38, 0x3000
	v_mad_u32_u16 v142, v69, v249, v144
	global_load_lds_dwordx4 v142, s[10:11]
	s_add_i32 m0, s38, 0x3400
	v_mad_u32_u16 v143, v73, v249, v145
	global_load_lds_dwordx4 v143, s[10:11]
	v_cvt_scalef32_pk_bf16_fp4 v98, v82, 1.0
	v_cvt_scalef32_pk_bf16_fp4 v99, v82, 1.0 op_sel:[1,0,0]
	v_cvt_scalef32_pk_bf16_fp4 v100, v82, 1.0 op_sel:[0,1,0]
	v_cvt_scalef32_pk_bf16_fp4 v101, v82, 1.0 op_sel:[1,1,0]
	v_cvt_scalef32_pk_bf16_fp4 v102, v83, 1.0
	v_cvt_scalef32_pk_bf16_fp4 v103, v83, 1.0 op_sel:[1,0,0]
	v_cvt_scalef32_pk_bf16_fp4 v104, v83, 1.0 op_sel:[0,1,0]
	v_cvt_scalef32_pk_bf16_fp4 v105, v83, 1.0 op_sel:[1,1,0]
	v_mfma_f32_16x16x32_bf16 v[130:133], v[34:37], v[98:101], 0
	v_cvt_scalef32_pk_bf16_fp4 v98, v84, 1.0
	v_cvt_scalef32_pk_bf16_fp4 v99, v84, 1.0 op_sel:[1,0,0]
	v_cvt_scalef32_pk_bf16_fp4 v100, v84, 1.0 op_sel:[0,1,0]
	v_cvt_scalef32_pk_bf16_fp4 v101, v84, 1.0 op_sel:[1,1,0]
	v_mfma_f32_16x16x32_bf16 v[130:133], v[38:41], v[102:105], v[130:133]
	v_cvt_scalef32_pk_bf16_fp4 v102, v85, 1.0
	v_cvt_scalef32_pk_bf16_fp4 v103, v85, 1.0 op_sel:[1,0,0]
	v_cvt_scalef32_pk_bf16_fp4 v104, v85, 1.0 op_sel:[0,1,0]
	v_cvt_scalef32_pk_bf16_fp4 v105, v85, 1.0 op_sel:[1,1,0]
	v_mfma_f32_16x16x32_bf16 v[130:133], v[42:45], v[98:101], v[130:133]
	v_cvt_scalef32_pk_bf16_fp4 v98, v86, 1.0
	v_cvt_scalef32_pk_bf16_fp4 v99, v86, 1.0 op_sel:[1,0,0]
	v_cvt_scalef32_pk_bf16_fp4 v100, v86, 1.0 op_sel:[0,1,0]
	v_cvt_scalef32_pk_bf16_fp4 v101, v86, 1.0 op_sel:[1,1,0]
	v_mfma_f32_16x16x32_bf16 v[130:133], v[46:49], v[102:105], v[130:133]
	v_cvt_scalef32_pk_bf16_fp4 v102, v87, 1.0
	v_cvt_scalef32_pk_bf16_fp4 v103, v87, 1.0 op_sel:[1,0,0]
	v_cvt_scalef32_pk_bf16_fp4 v104, v87, 1.0 op_sel:[0,1,0]
	v_cvt_scalef32_pk_bf16_fp4 v105, v87, 1.0 op_sel:[1,1,0]
	v_mfma_f32_16x16x32_bf16 v[130:133], v[50:53], v[98:101], v[130:133]
	v_cvt_scalef32_pk_bf16_fp4 v98, v88, 1.0
	v_cvt_scalef32_pk_bf16_fp4 v99, v88, 1.0 op_sel:[1,0,0]
	v_cvt_scalef32_pk_bf16_fp4 v100, v88, 1.0 op_sel:[0,1,0]
	v_cvt_scalef32_pk_bf16_fp4 v101, v88, 1.0 op_sel:[1,1,0]
	v_mfma_f32_16x16x32_bf16 v[130:133], v[54:57], v[102:105], v[130:133]
	v_cvt_scalef32_pk_bf16_fp4 v102, v89, 1.0
	v_cvt_scalef32_pk_bf16_fp4 v103, v89, 1.0 op_sel:[1,0,0]
	v_cvt_scalef32_pk_bf16_fp4 v104, v89, 1.0 op_sel:[0,1,0]
	v_cvt_scalef32_pk_bf16_fp4 v105, v89, 1.0 op_sel:[1,1,0]
	v_mfma_f32_16x16x32_bf16 v[130:133], v[58:61], v[98:101], v[130:133]
	v_mfma_f32_16x16x32_bf16 v[130:133], v[62:65], v[102:105], v[130:133]
	s_waitcnt vmcnt(12)
	ds_read_b128 v[82:85], v146
	ds_read_b128 v[86:89], v147
	s_waitcnt lgkmcnt(2)
	s_add_i32 m0, s38, 0x3800
	v_mad_u32_u16 v142, v69, v249, v144 op_sel:[1,0,0,0]
	global_load_lds_dwordx4 v142, s[10:11]
	s_add_i32 m0, s38, 0x3c00
	v_mad_u32_u16 v143, v73, v249, v145 op_sel:[1,0,0,0]
	global_load_lds_dwordx4 v143, s[10:11]
	ds_read_b128 v[2:5], v148
	ds_read_b128 v[6:9], v148 offset:16
	ds_read_b128 v[10:13], v148 offset:32
	ds_read_b128 v[14:17], v148 offset:48
	ds_read_b128 v[18:21], v148 offset:256
	ds_read_b128 v[22:25], v148 offset:272
	ds_read_b128 v[26:29], v148 offset:288
	ds_read_b128 v[30:33], v148 offset:304
	v_cvt_scalef32_pk_bf16_fp4 v98, v90, 1.0
	v_cvt_scalef32_pk_bf16_fp4 v99, v90, 1.0 op_sel:[1,0,0]
	v_cvt_scalef32_pk_bf16_fp4 v100, v90, 1.0 op_sel:[0,1,0]
	v_cvt_scalef32_pk_bf16_fp4 v101, v90, 1.0 op_sel:[1,1,0]
	v_cvt_scalef32_pk_bf16_fp4 v102, v91, 1.0
	v_cvt_scalef32_pk_bf16_fp4 v103, v91, 1.0 op_sel:[1,0,0]
	v_cvt_scalef32_pk_bf16_fp4 v104, v91, 1.0 op_sel:[0,1,0]
	v_cvt_scalef32_pk_bf16_fp4 v105, v91, 1.0 op_sel:[1,1,0]
	v_mfma_f32_16x16x32_bf16 v[134:137], v[34:37], v[98:101], 0
	v_cvt_scalef32_pk_bf16_fp4 v98, v92, 1.0
	v_cvt_scalef32_pk_bf16_fp4 v99, v92, 1.0 op_sel:[1,0,0]
	v_cvt_scalef32_pk_bf16_fp4 v100, v92, 1.0 op_sel:[0,1,0]
	v_cvt_scalef32_pk_bf16_fp4 v101, v92, 1.0 op_sel:[1,1,0]
	v_mfma_f32_16x16x32_bf16 v[134:137], v[38:41], v[102:105], v[134:137]
	v_cvt_scalef32_pk_bf16_fp4 v102, v93, 1.0
	v_cvt_scalef32_pk_bf16_fp4 v103, v93, 1.0 op_sel:[1,0,0]
	v_cvt_scalef32_pk_bf16_fp4 v104, v93, 1.0 op_sel:[0,1,0]
	v_cvt_scalef32_pk_bf16_fp4 v105, v93, 1.0 op_sel:[1,1,0]
	v_mfma_f32_16x16x32_bf16 v[134:137], v[42:45], v[98:101], v[134:137]
	v_cvt_scalef32_pk_bf16_fp4 v98, v94, 1.0
	v_cvt_scalef32_pk_bf16_fp4 v99, v94, 1.0 op_sel:[1,0,0]
	v_cvt_scalef32_pk_bf16_fp4 v100, v94, 1.0 op_sel:[0,1,0]
	v_cvt_scalef32_pk_bf16_fp4 v101, v94, 1.0 op_sel:[1,1,0]
	v_mfma_f32_16x16x32_bf16 v[134:137], v[46:49], v[102:105], v[134:137]
	v_cvt_scalef32_pk_bf16_fp4 v102, v95, 1.0
	v_cvt_scalef32_pk_bf16_fp4 v103, v95, 1.0 op_sel:[1,0,0]
	v_cvt_scalef32_pk_bf16_fp4 v104, v95, 1.0 op_sel:[0,1,0]
	v_cvt_scalef32_pk_bf16_fp4 v105, v95, 1.0 op_sel:[1,1,0]
	v_mfma_f32_16x16x32_bf16 v[134:137], v[50:53], v[98:101], v[134:137]
	v_cvt_scalef32_pk_bf16_fp4 v98, v96, 1.0
	v_cvt_scalef32_pk_bf16_fp4 v99, v96, 1.0 op_sel:[1,0,0]
	v_cvt_scalef32_pk_bf16_fp4 v100, v96, 1.0 op_sel:[0,1,0]
	v_cvt_scalef32_pk_bf16_fp4 v101, v96, 1.0 op_sel:[1,1,0]
	v_mfma_f32_16x16x32_bf16 v[134:137], v[54:57], v[102:105], v[134:137]
	v_cvt_scalef32_pk_bf16_fp4 v102, v97, 1.0
	v_cvt_scalef32_pk_bf16_fp4 v103, v97, 1.0 op_sel:[1,0,0]
	v_cvt_scalef32_pk_bf16_fp4 v104, v97, 1.0 op_sel:[0,1,0]
	v_cvt_scalef32_pk_bf16_fp4 v105, v97, 1.0 op_sel:[1,1,0]
	v_mfma_f32_16x16x32_bf16 v[134:137], v[58:61], v[98:101], v[134:137]
	v_cvt_pk_bf16_f32 v140, v122, v126
	v_mfma_f32_16x16x32_bf16 v[134:137], v[62:65], v[102:105], v[134:137]
	s_nop 7
	s_nop 7
	v_cvt_pk_bf16_f32 v141, v130, v134
	s_mov_b64 exec, 0xffff
	global_store_dwordx4 v151, v[138:141], s[4:5]
	s_mov_b64 exec, -1
	v_add_u32_e32 v151, s42, v151
	s_add_i32 s34, s34, 2
	s_cmp_lt_u32 s34, 8
	s_cbranch_scc1 .Le1_loop
	s_cmp_lt_i32 s35, 0
	s_cbranch_scc1 .Le1_exit
	s_add_i32 s39, s39, s43
	s_add_i32 s39, s39, 7
	s_mov_b32 s34, 0
	s_branch .Le1_loop
